# v11 + UT chain runs 7 units per sequence: the 8th unit's result was never stored or used (EpiUTScan stores only for n<7)
# baseline (speedup 1.0000x reference)
.LBB0_584:
	s_add_i32 s70, s70, 1
	s_mov_b64 s[34:35], s[8:9]
	s_add_i32 s8, s70, 1
	s_lshr_b32 s8, s8, 3
	v_readlane_b32 s9, v252, 57
	s_mul_i32 s8, s8, s9
	s_add_i32 s8, s8, s88
	s_cmpk_lt_i32 s8, 0x80
	s_cselect_b64 s[12:13], -1, 0
	s_lshl_b32 s9, s8, 2
	s_mov_b64 s[20:21], s[10:11]
	s_and_b32 s9, s9, 0x7ffffff8
	s_and_b32 s11, s70, 7
	s_or_b32 s9, s9, s11
	s_lshl_b32 s9, s9, 1
	s_and_b32 s8, s8, 1
	s_mov_b32 s10, s71
	s_mov_b32 s72, s71
	s_or_b32 s71, s9, s8
	s_and_b64 s[8:9], s[12:13], exec
	s_cselect_b32 s42, s71, s10
	s_ashr_i32 s8, s42, 1
	s_ashr_i32 s9, s8, 31
	s_lshl_b64 s[10:11], s[8:9], 19
	s_add_u32 s10, s6, s10
	s_addc_u32 s11, s7, s11
	s_lshl_b32 s42, s42, 18
	s_and_b32 s42, s42, 0x40000
	s_add_u32 s10, s10, s42
	s_addc_u32 s11, s11, 0
	s_and_b64 s[42:43], s[12:13], exec
	s_cselect_b32 s73, s11, s21
	s_cselect_b32 s74, s10, s20
	s_lshl_b64 s[8:9], s[8:9], 17
	s_add_u32 s8, s28, s8
	s_addc_u32 s9, s54, s9
	s_and_b64 s[42:43], s[12:13], exec
	s_cselect_b32 s75, s9, s35
	s_cselect_b32 s76, s8, s34
	s_mov_b64 s[42:43], -1
	s_mov_b64 s[44:45], 0
	s_mov_b32 s46, 0
